# v20 = v19 + the same output-line pairing for expert-down conversion tiles (RWKV-scan loader waves and the in0/in1 converter workgroups)
# baseline (speedup 1.0000x reference)
; __device__ __forceinline__ ConvTile conv_tile_desc(const unsigned long long* tab, int t) {
;     ...
;     else { const int u = (t < CT_TOTAL ? t : CT_TOTAL - 1) - CT_C; e = u / 7168; const int v = u % 7168; si = 9; di = 17; N = DM; K = EXD; nb = v & 31; kb = v >> 5; }
;     const int n0 = nb * 64;
;     int col0 = n0, nvalid = 64;
;     if (mode) { col0 = (n0 >> 8) * 128 + (n0 & 127); si += (n0 >> 7) & 1; }
;     if (npad) { nvalid = N - n0; if (nvalid <= 0) col0 = 0; }
;     ConvTile c;
;     const size_t KN = (size_t)K * N;
;     c.src = (const float*)tab[si] + (size_t)e * KN + (size_t)(kb * 32) * N + col0;
;     c.dst = (bf16_t*)tab[di] + (size_t)e * (mode ? 2 * KN : KN) + (size_t)n0 * K + kb * 32;
;     c.N = N; c.K = K; c.nvalid = nvalid;
;     return c;
; }
.Lcv0_start:
	v_and_b32_e32 v96, 63, v0
	v_lshrrev_b32_e32 v97, 6, v0
	v_lshrrev_b32_e32 v98, 4, v96
	v_and_b32_e32 v99, 15, v96
	v_readfirstlane_b32 s2, v97
	v_lshlrev_b32_e32 v100, 16, v98
	v_lshl_add_u32 v100, v99, 4, v100
	v_add_u32_e32 v101, 0x2000, v100
	v_add_u32_e32 v102, 0x4000, v100
	v_add_u32_e32 v103, 0x6000, v100
	v_add_u32_e32 v104, 0x8000, v100
	v_add_u32_e32 v105, 0xa000, v100
	v_add_u32_e32 v106, 0xc000, v100
	v_add_u32_e32 v107, 0xe000, v100
	v_mul_u32_u24_e32 v108, 0xe000, v99
	v_lshl_add_u32 v108, v98, 4, v108
	v_add_u32_e32 v109, 0x3800, v108
	v_add_u32_e32 v110, 0x7000, v108
	v_add_u32_e32 v111, 0xa800, v108
	v_mov_b32_e32 v112, 0x20088
	v_mov_b32_e32 v113, 0x200c8
	ds_read_b64 v[114:115], v112
	ds_read_b64 v[116:117], v113
	s_waitcnt lgkmcnt(0)
	v_readfirstlane_b32 s4, v114
	v_readfirstlane_b32 s5, v115
	v_readfirstlane_b32 s6, v116
	v_readfirstlane_b32 s7, v117
	s_sub_i32 s3, s90, 224
	s_lshl_b32 s3, s3, 3
	s_add_i32 s3, s3, s2
	s_add_i32 s3, s3, 0x2ac00
	s_nop 4
	s_min_u32 s12, s3, 0x324ff
	s_sub_u32 s12, s12, 0x24500
	s_lshr_b32 s13, s12, 10
	s_mul_i32 s13, s13, 37
	s_lshr_b32 s13, s13, 8
	s_mul_i32 s28, s13, 0x1c00
	s_sub_u32 s12, s12, s28
	s_bfe_u32 s28, s12, 0x50001
	s_and_b32 s32, s12, 1
	s_lshr_b32 s12, s12, 6
	s_lshl_b32 s12, s12, 1
	s_or_b32 s12, s12, s32
	s_mul_i32 s29, s13, 0x3800000
	s_lshl_b32 s32, s12, 18
	s_add_u32 s29, s29, s32
	s_lshl_b32 s32, s28, 8
	s_add_u32 s29, s29, s32
	s_add_u32 s8, s4, s29
	s_addc_u32 s9, s5, 0
	s_mul_i32 s29, s13, 0x1c00000
	s_mul_i32 s32, s28, 0xe0000
	s_add_u32 s29, s29, s32
	s_lshl_b32 s32, s12, 6
	s_add_u32 s29, s29, s32
	s_add_u32 s10, s6, s29
	s_addc_u32 s11, s7, 0
	s_nop 0
	global_load_dwordx4 v[128:131], v100, s[8:9] nt
	global_load_dwordx4 v[132:135], v101, s[8:9] nt
	global_load_dwordx4 v[136:139], v102, s[8:9] nt
	global_load_dwordx4 v[140:143], v103, s[8:9] nt
	global_load_dwordx4 v[144:147], v104, s[8:9] nt
	global_load_dwordx4 v[148:151], v105, s[8:9] nt
	global_load_dwordx4 v[152:155], v106, s[8:9] nt
	global_load_dwordx4 v[156:159], v107, s[8:9] nt
	s_add_i32 s3, s3, 256
	s_min_u32 s12, s3, 0x324ff
	s_sub_u32 s12, s12, 0x24500
	s_lshr_b32 s13, s12, 10
	s_mul_i32 s13, s13, 37
	s_lshr_b32 s13, s13, 8
	s_mul_i32 s28, s13, 0x1c00
	s_sub_u32 s12, s12, s28
	s_bfe_u32 s28, s12, 0x50001
	s_and_b32 s32, s12, 1
	s_lshr_b32 s12, s12, 6
	s_lshl_b32 s12, s12, 1
	s_or_b32 s12, s12, s32
	s_mul_i32 s29, s13, 0x3800000
	s_lshl_b32 s32, s12, 18
	s_add_u32 s29, s29, s32
	s_lshl_b32 s32, s28, 8
	s_add_u32 s29, s29, s32
	s_add_u32 s8, s4, s29
	s_addc_u32 s9, s5, 0
	s_mul_i32 s29, s13, 0x1c00000
	s_mul_i32 s32, s28, 0xe0000
	s_add_u32 s29, s29, s32
	s_lshl_b32 s32, s12, 6
	s_add_u32 s29, s29, s32
	s_add_u32 s36, s6, s29
	s_addc_u32 s37, s7, 0
	s_nop 0
	global_load_dwordx4 v[64:67], v100, s[8:9] nt
	global_load_dwordx4 v[68:71], v101, s[8:9] nt
	global_load_dwordx4 v[72:75], v102, s[8:9] nt
	global_load_dwordx4 v[76:79], v103, s[8:9] nt
	global_load_dwordx4 v[80:83], v104, s[8:9] nt
	global_load_dwordx4 v[84:87], v105, s[8:9] nt
	global_load_dwordx4 v[88:91], v106, s[8:9] nt
	global_load_dwordx4 v[92:95], v107, s[8:9] nt
	s_waitcnt vmcnt(8)
	v_cvt_pk_bf16_f32 v112, v128, v132
	v_cvt_pk_bf16_f32 v113, v136, v140
	v_cvt_pk_bf16_f32 v114, v144, v148
	v_cvt_pk_bf16_f32 v115, v152, v156
	global_store_dwordx4 v108, v[112:115], s[10:11] nt
	v_cvt_pk_bf16_f32 v116, v129, v133
	v_cvt_pk_bf16_f32 v117, v137, v141
	v_cvt_pk_bf16_f32 v118, v145, v149
	v_cvt_pk_bf16_f32 v119, v153, v157
	global_store_dwordx4 v109, v[116:119], s[10:11] nt
	v_cvt_pk_bf16_f32 v120, v130, v134
	v_cvt_pk_bf16_f32 v121, v138, v142
	v_cvt_pk_bf16_f32 v122, v146, v150
	v_cvt_pk_bf16_f32 v123, v154, v158
	global_store_dwordx4 v110, v[120:123], s[10:11] nt
	v_cvt_pk_bf16_f32 v96, v131, v135
	v_cvt_pk_bf16_f32 v97, v139, v143
	v_cvt_pk_bf16_f32 v98, v147, v151
	v_cvt_pk_bf16_f32 v99, v155, v159
	global_store_dwordx4 v111, v[96:99], s[10:11] nt
	s_movk_i32 s33, 27
; __device__ __forceinline__ ConvTile conv_tile_desc(const unsigned long long* tab, int t) {
;     ...
;     else { const int u = (t < CT_TOTAL ? t : CT_TOTAL - 1) - CT_C; e = u / 7168; const int v = u % 7168; si = 9; di = 17; N = DM; K = EXD; nb = v & 31; kb = v >> 5; }
;     const int n0 = nb * 64;
;     int col0 = n0, nvalid = 64;
;     if (mode) { col0 = (n0 >> 8) * 128 + (n0 & 127); si += (n0 >> 7) & 1; }
;     if (npad) { nvalid = N - n0; if (nvalid <= 0) col0 = 0; }
;     ConvTile c;
;     const size_t KN = (size_t)K * N;
;     c.src = (const float*)tab[si] + (size_t)e * KN + (size_t)(kb * 32) * N + col0;
;     c.dst = (bf16_t*)tab[di] + (size_t)e * (mode ? 2 * KN : KN) + (size_t)n0 * K + kb * 32;
;     c.N = N; c.K = K; c.nvalid = nvalid;
;     return c;
; }
.Lcv0_loop:
	s_add_i32 s3, s3, 256
	s_min_u32 s12, s3, 0x324ff
	s_sub_u32 s12, s12, 0x24500
	s_lshr_b32 s13, s12, 10
	s_mul_i32 s13, s13, 37
	s_lshr_b32 s13, s13, 8
	s_mul_i32 s28, s13, 0x1c00
	s_sub_u32 s12, s12, s28
	s_bfe_u32 s28, s12, 0x50001
	s_and_b32 s32, s12, 1
	s_lshr_b32 s12, s12, 6
	s_lshl_b32 s12, s12, 1
	s_or_b32 s12, s12, s32
	s_mul_i32 s29, s13, 0x3800000
	s_lshl_b32 s32, s12, 18
	s_add_u32 s29, s29, s32
	s_lshl_b32 s32, s28, 8
	s_add_u32 s29, s29, s32
	s_add_u32 s8, s4, s29
	s_addc_u32 s9, s5, 0
	s_mul_i32 s29, s13, 0x1c00000
	s_mul_i32 s32, s28, 0xe0000
	s_add_u32 s29, s29, s32
	s_lshl_b32 s32, s12, 6
	s_add_u32 s29, s29, s32
	s_add_u32 s10, s6, s29
	s_addc_u32 s11, s7, 0
	s_nop 0
	global_load_dwordx4 v[128:131], v100, s[8:9] nt
	global_load_dwordx4 v[132:135], v101, s[8:9] nt
	global_load_dwordx4 v[136:139], v102, s[8:9] nt
	global_load_dwordx4 v[140:143], v103, s[8:9] nt
	global_load_dwordx4 v[144:147], v104, s[8:9] nt
	global_load_dwordx4 v[148:151], v105, s[8:9] nt
	global_load_dwordx4 v[152:155], v106, s[8:9] nt
	global_load_dwordx4 v[156:159], v107, s[8:9] nt
	s_waitcnt vmcnt(12)
	v_cvt_pk_bf16_f32 v112, v64, v68
	v_cvt_pk_bf16_f32 v113, v72, v76
	v_cvt_pk_bf16_f32 v114, v80, v84
	v_cvt_pk_bf16_f32 v115, v88, v92
	global_store_dwordx4 v108, v[112:115], s[36:37] nt
	v_cvt_pk_bf16_f32 v116, v65, v69
	v_cvt_pk_bf16_f32 v117, v73, v77
	v_cvt_pk_bf16_f32 v118, v81, v85
	v_cvt_pk_bf16_f32 v119, v89, v93
	global_store_dwordx4 v109, v[116:119], s[36:37] nt
	v_cvt_pk_bf16_f32 v120, v66, v70
	v_cvt_pk_bf16_f32 v121, v74, v78
	v_cvt_pk_bf16_f32 v122, v82, v86
	v_cvt_pk_bf16_f32 v123, v90, v94
	global_store_dwordx4 v110, v[120:123], s[36:37] nt
	v_cvt_pk_bf16_f32 v96, v67, v71
	v_cvt_pk_bf16_f32 v97, v75, v79
	v_cvt_pk_bf16_f32 v98, v83, v87
	v_cvt_pk_bf16_f32 v99, v91, v95
	global_store_dwordx4 v111, v[96:99], s[36:37] nt
	s_add_i32 s3, s3, 256
	s_min_u32 s12, s3, 0x324ff
	s_sub_u32 s12, s12, 0x24500
	s_lshr_b32 s13, s12, 10
	s_mul_i32 s13, s13, 37
	s_lshr_b32 s13, s13, 8
	s_mul_i32 s28, s13, 0x1c00
	s_sub_u32 s12, s12, s28
	s_bfe_u32 s28, s12, 0x50001
	s_and_b32 s32, s12, 1
	s_lshr_b32 s12, s12, 6
	s_lshl_b32 s12, s12, 1
	s_or_b32 s12, s12, s32
	s_mul_i32 s29, s13, 0x3800000
	s_lshl_b32 s32, s12, 18
	s_add_u32 s29, s29, s32
	s_lshl_b32 s32, s28, 8
	s_add_u32 s29, s29, s32
	s_add_u32 s8, s4, s29
	s_addc_u32 s9, s5, 0
	s_mul_i32 s29, s13, 0x1c00000
	s_mul_i32 s32, s28, 0xe0000
	s_add_u32 s29, s29, s32
	s_lshl_b32 s32, s12, 6
	s_add_u32 s29, s29, s32
	s_add_u32 s36, s6, s29
	s_addc_u32 s37, s7, 0
	s_nop 0
	global_load_dwordx4 v[64:67], v100, s[8:9] nt
	global_load_dwordx4 v[68:71], v101, s[8:9] nt
	global_load_dwordx4 v[72:75], v102, s[8:9] nt
	global_load_dwordx4 v[76:79], v103, s[8:9] nt
	global_load_dwordx4 v[80:83], v104, s[8:9] nt
	global_load_dwordx4 v[84:87], v105, s[8:9] nt
	global_load_dwordx4 v[88:91], v106, s[8:9] nt
	global_load_dwordx4 v[92:95], v107, s[8:9] nt
	s_waitcnt vmcnt(12)
	v_cvt_pk_bf16_f32 v112, v128, v132
	v_cvt_pk_bf16_f32 v113, v136, v140
	v_cvt_pk_bf16_f32 v114, v144, v148
	v_cvt_pk_bf16_f32 v115, v152, v156
	global_store_dwordx4 v108, v[112:115], s[10:11] nt
	v_cvt_pk_bf16_f32 v116, v129, v133
	v_cvt_pk_bf16_f32 v117, v137, v141
	v_cvt_pk_bf16_f32 v118, v145, v149
	v_cvt_pk_bf16_f32 v119, v153, v157
	global_store_dwordx4 v109, v[116:119], s[10:11] nt
	v_cvt_pk_bf16_f32 v120, v130, v134
	v_cvt_pk_bf16_f32 v121, v138, v142
	v_cvt_pk_bf16_f32 v122, v146, v150
	v_cvt_pk_bf16_f32 v123, v154, v158
	global_store_dwordx4 v110, v[120:123], s[10:11] nt
	v_cvt_pk_bf16_f32 v96, v131, v135
	v_cvt_pk_bf16_f32 v97, v139, v143
	v_cvt_pk_bf16_f32 v98, v147, v151
	v_cvt_pk_bf16_f32 v99, v155, v159
	global_store_dwordx4 v111, v[96:99], s[10:11] nt
	s_sub_i32 s33, s33, 1
	s_cmp_lg_u32 s33, 0
	s_cbranch_scc1 .Lcv0_loop
	s_waitcnt vmcnt(4)
	v_cvt_pk_bf16_f32 v112, v64, v68
	v_cvt_pk_bf16_f32 v113, v72, v76
	v_cvt_pk_bf16_f32 v114, v80, v84
	v_cvt_pk_bf16_f32 v115, v88, v92
	global_store_dwordx4 v108, v[112:115], s[36:37] nt
	v_cvt_pk_bf16_f32 v116, v65, v69
	v_cvt_pk_bf16_f32 v117, v73, v77
	v_cvt_pk_bf16_f32 v118, v81, v85
	v_cvt_pk_bf16_f32 v119, v89, v93
	global_store_dwordx4 v109, v[116:119], s[36:37] nt
	v_cvt_pk_bf16_f32 v120, v66, v70
	v_cvt_pk_bf16_f32 v121, v74, v78
	v_cvt_pk_bf16_f32 v122, v82, v86
	v_cvt_pk_bf16_f32 v123, v90, v94
	global_store_dwordx4 v110, v[120:123], s[36:37] nt
	v_cvt_pk_bf16_f32 v96, v67, v71
	v_cvt_pk_bf16_f32 v97, v75, v79
	v_cvt_pk_bf16_f32 v98, v83, v87
	v_cvt_pk_bf16_f32 v99, v91, v95
	global_store_dwordx4 v111, v[96:99], s[36:37] nt
	s_branch .LBB0_237

; #define CT_LOADNT(T_) do { const int tt_ = (T_) < CT_TOTAL ? (T_) : CT_TOTAL - 1; const ConvTile ct_ = conv_tile_desc(cttab, tt_); const int ckq_ = lane >> 4, ccol_ = ((lane & 15) * 4 < ct_.nvalid) ? (lane & 15) * 4 : 0; CT_FORQ(CT_LOAD1NT) } while (0)
; __device__ __forceinline__ void ph_rwscan(const Params& p, float* lds, int wg, int nwg, int ct_begin) {
;     ...
;         float* buf0 = lds; float* buf1 = lds + RW_TB * RW_STEPF;
;         float4 cv0, cv1, cv2, cv3, cv4, cv5, cv6, cv7;
;         const unsigned long long* cttab = (const unsigned long long*)((const char*)lds + CTTAB_OFF);
;         const int cgw = wg * 4 + (wave - 4), cnw = nwg * 4;
;         char* const ctlds = (char*)lds + 2 * RW_TB * RW_STEPF * 4 + (wave - 4) * CT_LDS_BYTES;
;         if (loader) { RW_LOAD_BLOCK(0, A); RW_WRITE_BLOCK(buf0, A); RW_LOAD_BLOCK(1, A); RW_LOAD_BLOCK(2, B); CT_LOADNT(ct_begin + cgw); }
;         __syncthreads();
;         f2v Sa = {0.f, 0.f}, Sb = {0.f, 0.f};
;         float* const Yd = dir ? p.Y[1] : p.Y[0];
;         const int seg = lane & 15, vrl = wave * 4 + (lane >> 4);
.LBB0_628:
	s_andn2_b64 vcc, exec, s[56:57]
	s_cbranch_vccnz .LBB0_684
	s_setprio 0
	s_waitcnt vmcnt(0)
	ds_write_b128 v175, v[6:9] offset:43008
	ds_write_b128 v176, v[10:13] offset:43008
	v_lshlrev_b32_e32 v6, 16, v34
	v_and_b32_e32 v7, 0xffff0000, v34
	v_lshlrev_b32_e32 v8, 16, v35
	v_and_b32_e32 v9, 0xffff0000, v35
	ds_write_b128 v177, v[6:9] offset:43024
	v_lshlrev_b32_e32 v6, 16, v36
	v_and_b32_e32 v7, 0xffff0000, v36
	v_lshlrev_b32_e32 v8, 16, v37
	v_and_b32_e32 v9, 0xffff0000, v37
	ds_write_b128 v177, v[6:9] offset:43104
	v_lshlrev_b32_e32 v6, 16, v26
	v_and_b32_e32 v7, 0xffff0000, v26
	v_lshlrev_b32_e32 v8, 16, v27
	v_and_b32_e32 v9, 0xffff0000, v27
	ds_write_b128 v177, v[6:9] offset:43040
	v_lshlrev_b32_e32 v6, 16, v28
	v_and_b32_e32 v7, 0xffff0000, v28
	v_lshlrev_b32_e32 v8, 16, v29
	v_and_b32_e32 v9, 0xffff0000, v29
	s_min_u32 s56, s79, 0x84
	ds_write_b128 v177, v[6:9] offset:43120
	v_lshlrev_b32_e32 v6, 16, v18
	v_and_b32_e32 v7, 0xffff0000, v18
	v_lshlrev_b32_e32 v8, 16, v19
	v_and_b32_e32 v9, 0xffff0000, v19
	s_lshl_b32 s56, s56, 5
	ds_write_b128 v177, v[6:9] offset:43056
	v_lshlrev_b32_e32 v6, 16, v20
	v_and_b32_e32 v7, 0xffff0000, v20
	v_lshlrev_b32_e32 v8, 16, v21
	v_and_b32_e32 v9, 0xffff0000, v21
	s_cmp_lt_u32 s79, 5
	s_movk_i32 s59, 0x60
	ds_write_b128 v177, v[6:9] offset:43136
	v_lshlrev_b32_e32 v6, 16, v14
	v_and_b32_e32 v7, 0xffff0000, v14
	v_lshlrev_b32_e32 v8, 16, v15
	v_and_b32_e32 v9, 0xffff0000, v15
	s_cselect_b32 s59, s59, 0xffffff60
	ds_write_b128 v177, v[6:9] offset:43072
	v_lshlrev_b32_e32 v6, 16, v16
	v_and_b32_e32 v7, 0xffff0000, v16
	v_lshlrev_b32_e32 v8, 16, v17
	v_and_b32_e32 v9, 0xffff0000, v17
	s_cselect_b32 s57, s81, 0x1000
	s_cselect_b32 s58, s3, s78
	s_add_i32 s56, s56, s59
	ds_write_b128 v177, v[6:9] offset:43152
	ds_write_b128 v178, v[2:5] offset:44288
	v_or_b32_e32 v2, s56, v131
	v_xad_u32 v3, v2, -1, s57
	v_cndmask_b32_e64 v2, v3, v2, s[38:39]
	v_or_b32_e32 v3, s56, v135
	v_xad_u32 v4, v3, -1, s57
	v_cndmask_b32_e64 v4, v4, v3, s[38:39]
	v_or_b32_e32 v3, s56, v141
	v_xad_u32 v5, v3, -1, s57
	v_cndmask_b32_e64 v6, v5, v3, s[38:39]
	v_or_b32_e32 v3, s56, v161
	v_xad_u32 v5, v3, -1, s57
	v_add_u32_e32 v2, s58, v2
	v_add_u32_e32 v6, s58, v6
	v_cndmask_b32_e64 v8, v5, v3, s[38:39]
	v_ashrrev_i32_e32 v3, 31, v2
	v_add_u32_e32 v4, s58, v4
	v_ashrrev_i32_e32 v7, 31, v6
	v_ashrrev_i32_e32 v5, 31, v4
	v_lshlrev_b64 v[6:7], 10, v[6:7]
	v_lshlrev_b64 v[2:3], 12, v[2:3]
	v_lshl_add_u64 v[14:15], v[6:7], 0, v[150:151]
	v_add_u32_e32 v90, s58, v8
	v_lshl_add_u64 v[2:3], v[152:153], 0, v[2:3]
	v_lshlrev_b64 v[4:5], 12, v[4:5]
	v_readlane_b32 s56, v246, 16
	v_lshl_add_u64 v[4:5], v[152:153], 0, v[4:5]
	global_load_dwordx4 v[6:9], v[2:3], off
	global_load_dwordx4 v[10:13], v[4:5], off
	v_lshlrev_b64 v[2:3], 1, v[14:15]
	v_readlane_b32 s66, v246, 26
	v_readlane_b32 s67, v246, 27
	v_readlane_b32 s62, v246, 22
	v_readlane_b32 s63, v246, 23
	v_lshl_add_u64 v[4:5], s[66:67], 0, v[2:3]
	global_load_dwordx4 v[34:37], v[4:5], off
	v_lshl_add_u64 v[4:5], s[84:85], 0, v[2:3]
	v_ashrrev_i32_e32 v91, 31, v90
	global_load_dwordx4 v[26:29], v[4:5], off
	v_lshl_add_u64 v[4:5], s[92:93], 0, v[2:3]
	v_lshl_add_u64 v[2:3], s[62:63], 0, v[2:3]
	global_load_dwordx4 v[14:17], v[2:3], off
	v_lshlrev_b64 v[2:3], 12, v[90:91]
	v_lshl_add_u64 v[2:3], v[154:155], 0, v[2:3]
	global_load_dwordx4 v[18:21], v[4:5], off
	s_min_i32 s72, s33, 0x324ff
	global_load_dwordx4 v[2:5], v[2:3], off
	v_readlane_b32 s57, v246, 17
	v_readlane_b32 s58, v246, 18
	v_readlane_b32 s59, v246, 19
	v_readlane_b32 s60, v246, 20
	v_readlane_b32 s61, v246, 21
	v_readlane_b32 s64, v246, 24
	v_readlane_b32 s65, v246, 25
	s_cmpk_gt_i32 s33, 0x19ff
	s_mov_b64 s[62:63], -1
	v_readlane_b32 s68, v246, 28
	v_readlane_b32 s69, v246, 29
	v_readlane_b32 s70, v246, 30
	v_readlane_b32 s71, v246, 31
	s_cbranch_scc0 .LBB0_654
	s_cmpk_gt_u32 s33, 0x21ff
	s_cbranch_scc0 .LBB0_651
	s_cmpk_gt_u32 s33, 0x4dff
	s_cbranch_scc0 .LBB0_648
	s_cmpk_gt_u32 s33, 0x63ff
	s_cbranch_scc0 .LBB0_645
	s_mov_b64 s[58:59], -1
	s_cmpk_gt_u32 s33, 0x7cff
	s_cbranch_scc0 .LBB0_642
	s_cmpk_gt_u32 s33, 0x84ff
	s_cbranch_scc0 .LBB0_639
	s_cmp_gt_u32 s33, 0x244ff
	s_mov_b64 s[56:57], -1
	s_cbranch_scc0 .LBB0_637
	s_add_i32 s56, s72, 0xbb00
	s_bfe_u32 s57, s56, 0x6000a
	s_mulk_i32 s57, 0x2493
	s_lshr_b32 s74, s57, 16
	s_mul_i32 s57, s74, 0x1c00
	s_sub_i32 s56, s56, s57
	s_bfe_u32 s65, s56, 0x50001
	s_bfe_u32 s64, s56, 0xa0006
	s_lshl_b32 s64, s64, 1
	s_and_b32 s56, s56, 1
	s_or_b32 s64, s64, s56
	s_mov_b64 s[56:57], 0

; __device__ __forceinline__ ConvTile conv_tile_desc(const unsigned long long* tab, int t) {
;     ...
;     else { const int u = (t < CT_TOTAL ? t : CT_TOTAL - 1) - CT_C; e = u / 7168; const int v = u % 7168; si = 9; di = 17; N = DM; K = EXD; nb = v & 31; kb = v >> 5; }
;     const int n0 = nb * 64;
;     int col0 = n0, nvalid = 64;
;     if (mode) { col0 = (n0 >> 8) * 128 + (n0 & 127); si += (n0 >> 7) & 1; }
;     if (npad) { nvalid = N - n0; if (nvalid <= 0) col0 = 0; }
;     ConvTile c;
;     const size_t KN = (size_t)K * N;
;     c.src = (const float*)tab[si] + (size_t)e * KN + (size_t)(kb * 32) * N + col0;
;     c.dst = (bf16_t*)tab[di] + (size_t)e * (mode ? 2 * KN : KN) + (size_t)n0 * K + kb * 32;
.LBB0_656:
	s_lshl_b32 s62, s65, 6
	s_sub_i32 s61, s96, s62
	s_and_b64 s[58:59], s[58:59], exec
	s_cselect_b32 s63, 64, s61
	s_lshl_b32 s58, s75, 3
	s_add_i32 s58, s58, 0
	s_add_i32 s58, s58, 0x20040
	v_mov_b32_e32 v90, s58
	s_mul_i32 s72, s56, s96
	ds_read_b64 v[90:91], v90
	s_lshl_b64 s[58:59], s[72:73], s60
	s_lshl_b32 s60, s64, 5
	s_mul_i32 s59, s59, s74
	s_mul_hi_u32 s64, s58, s74
	s_add_i32 s59, s64, s59
	s_mul_i32 s58, s58, s74
	s_lshl_b64 s[58:59], s[58:59], 1
	s_waitcnt lgkmcnt(0)
	v_lshl_add_u64 v[90:91], v[90:91], 0, s[58:59]
	s_ashr_i32 s58, s62, 31
	s_mul_i32 s58, s56, s58
	s_mul_hi_u32 s59, s56, s62
	s_add_i32 s58, s59, s58
	s_mul_i32 s59, s57, s62
	s_add_i32 s59, s58, s59
	s_mul_i32 s58, s56, s62
	s_ashr_i32 s61, s60, 31
	s_lshl_b64 s[58:59], s[58:59], 1
	v_lshl_add_u64 v[90:91], v[90:91], 0, s[58:59]
	s_lshl_b64 s[58:59], s[60:61], 1
	v_mul_u32_u24_e32 v92, s56, v130
	v_lshl_add_u64 v[90:91], v[90:91], 0, s[58:59]
	v_lshlrev_b32_e32 v132, 1, v92
	v_lshl_add_u64 v[90:91], v[90:91], 0, v[132:133]
	v_lshlrev_b32_e32 v132, 1, v140
	v_cvt_pk_bf16_f32 v58, v58, v62
	v_cvt_pk_bf16_f32 v62, v66, v70
	v_cvt_pk_bf16_f32 v66, v74, v78
	v_cvt_pk_bf16_f32 v70, v82, v86
	v_cmp_gt_i32_e32 vcc, s63, v130
	v_lshl_add_u64 v[94:95], v[90:91], 0, v[132:133]
	s_lshl_b64 s[56:57], s[56:57], 1
	v_cndmask_b32_e32 v93, 0, v70, vcc
	v_cndmask_b32_e32 v92, 0, v66, vcc
	v_cndmask_b32_e32 v91, 0, v62, vcc
	v_cndmask_b32_e32 v90, 0, v58, vcc
	v_cvt_pk_bf16_f32 v58, v59, v63
	v_cvt_pk_bf16_f32 v59, v67, v71
	v_cvt_pk_bf16_f32 v62, v75, v79
	v_cvt_pk_bf16_f32 v63, v83, v87
	global_store_dwordx4 v[94:95], v[90:93], off nt
	v_cvt_pk_bf16_f32 v60, v60, v64
	v_cvt_pk_bf16_f32 v64, v84, v88
	v_cndmask_b32_e32 v93, 0, v63, vcc
	v_cndmask_b32_e32 v92, 0, v62, vcc
	v_cndmask_b32_e32 v91, 0, v59, vcc
	v_cndmask_b32_e32 v90, 0, v58, vcc
	v_lshl_add_u64 v[58:59], v[94:95], 0, s[56:57]
	v_cvt_pk_bf16_f32 v62, v68, v72
	v_cvt_pk_bf16_f32 v63, v76, v80
	s_add_i32 s65, s80, s33
	global_store_dwordx4 v[58:59], v[90:93], off nt
	s_min_i32 s72, s65, 0x324ff
	s_cmpk_gt_i32 s65, 0x19ff
	v_cndmask_b32_e32 v93, 0, v64, vcc
	v_cndmask_b32_e32 v92, 0, v63, vcc
	v_cndmask_b32_e32 v91, 0, v62, vcc
	v_cndmask_b32_e32 v90, 0, v60, vcc
	v_lshl_add_u64 v[62:63], v[58:59], 0, s[56:57]
	v_cvt_pk_bf16_f32 v58, v61, v65
	v_cvt_pk_bf16_f32 v59, v69, v73
	v_cvt_pk_bf16_f32 v60, v77, v81
	v_cvt_pk_bf16_f32 v61, v85, v89
	global_store_dwordx4 v[62:63], v[90:93], off nt
	v_cndmask_b32_e32 v61, 0, v61, vcc
	v_cndmask_b32_e32 v60, 0, v60, vcc
	v_cndmask_b32_e32 v59, 0, v59, vcc
	v_cndmask_b32_e32 v58, 0, v58, vcc
	v_lshl_add_u64 v[62:63], v[62:63], 0, s[56:57]
	s_mov_b64 s[96:97], -1
	global_store_dwordx4 v[62:63], v[58:61], off nt
	s_cbranch_scc0 .LBB0_681
	s_cmpk_gt_u32 s65, 0x21ff
	s_cbranch_scc0 .LBB0_678
	s_cmpk_gt_u32 s65, 0x4dff
	s_cbranch_scc0 .LBB0_675
	s_cmpk_gt_u32 s65, 0x63ff
	s_cbranch_scc0 .LBB0_672
	s_mov_b64 s[58:59], -1
	s_cmpk_gt_u32 s65, 0x7cff
	s_cbranch_scc0 .LBB0_669
	s_cmpk_gt_u32 s65, 0x84ff
	s_cbranch_scc0 .LBB0_666
	s_mov_b64 s[60:61], -1
	s_cmp_gt_u32 s65, 0x244ff
	s_mov_b64 s[56:57], -1
	s_cbranch_scc0 .LBB0_664
	s_add_i32 s56, s72, 0xbb00
	s_bfe_u32 s57, s56, 0x6000a
	s_mulk_i32 s57, 0x2493
	s_lshr_b32 s64, s57, 16
	s_mul_i32 s57, s64, 0x1c00
	s_sub_i32 s56, s56, s57
	s_bfe_u32 s75, s56, 0x50001
	s_bfe_u32 s74, s56, 0xa0006
	s_lshl_b32 s74, s74, 1
	s_and_b32 s56, s56, 1
	s_or_b32 s74, s74, s56
	s_mov_b64 s[56:57], 0

; #define CT_LOADNT(T_) do { const int tt_ = (T_) < CT_TOTAL ? (T_) : CT_TOTAL - 1; const ConvTile ct_ = conv_tile_desc(cttab, tt_); const int ckq_ = lane >> 4, ccol_ = ((lane & 15) * 4 < ct_.nvalid) ? (lane & 15) * 4 : 0; CT_FORQ(CT_LOAD1NT) } while (0)
; __device__ __forceinline__ void ph_rwscan(const Params& p, float* lds, int wg, int nwg, int ct_begin) {
;     ...
;         float* buf0 = lds; float* buf1 = lds + RW_TB * RW_STEPF;
;         float4 cv0, cv1, cv2, cv3, cv4, cv5, cv6, cv7;
;         const unsigned long long* cttab = (const unsigned long long*)((const char*)lds + CTTAB_OFF);
;         const int cgw = wg * 4 + (wave - 4), cnw = nwg * 4;
;         char* const ctlds = (char*)lds + 2 * RW_TB * RW_STEPF * 4 + (wave - 4) * CT_LDS_BYTES;
;         if (loader) { RW_LOAD_BLOCK(0, A); RW_WRITE_BLOCK(buf0, A); RW_LOAD_BLOCK(1, A); RW_LOAD_BLOCK(2, B); CT_LOADNT(ct_begin + cgw); }
;         __syncthreads();
;         f2v Sa = {0.f, 0.f}, Sb = {0.f, 0.f};
;         float* const Yd = dir ? p.Y[1] : p.Y[0];
;         const int seg = lane & 15, vrl = wave * 4 + (lane >> 4);
.LBB0_687:
	s_andn2_b64 vcc, exec, s[56:57]
	s_cbranch_vccnz .LBB0_743
	s_setprio 0
	s_waitcnt vmcnt(0)
	ds_write_b128 v175, v[30:33]
	ds_write_b128 v176, v[38:41]
	v_lshlrev_b32_e32 v30, 16, v54
	v_and_b32_e32 v31, 0xffff0000, v54
	v_lshlrev_b32_e32 v32, 16, v55
	v_and_b32_e32 v33, 0xffff0000, v55
	ds_write_b128 v177, v[30:33] offset:16
	v_lshlrev_b32_e32 v30, 16, v56
	v_and_b32_e32 v31, 0xffff0000, v56
	v_lshlrev_b32_e32 v32, 16, v57
	v_and_b32_e32 v33, 0xffff0000, v57
	ds_write_b128 v177, v[30:33] offset:96
	v_lshlrev_b32_e32 v30, 16, v50
	v_and_b32_e32 v31, 0xffff0000, v50
	v_lshlrev_b32_e32 v32, 16, v51
	v_and_b32_e32 v33, 0xffff0000, v51
	ds_write_b128 v177, v[30:33] offset:32
	v_lshlrev_b32_e32 v30, 16, v52
	v_and_b32_e32 v31, 0xffff0000, v52
	v_lshlrev_b32_e32 v32, 16, v53
	v_and_b32_e32 v33, 0xffff0000, v53
	s_min_u32 s56, s79, 0x83
	ds_write_b128 v177, v[30:33] offset:112
	v_lshlrev_b32_e32 v30, 16, v46
	v_and_b32_e32 v31, 0xffff0000, v46
	v_lshlrev_b32_e32 v32, 16, v47
	v_and_b32_e32 v33, 0xffff0000, v47
	s_lshl_b32 s56, s56, 5
	ds_write_b128 v177, v[30:33] offset:48
	v_lshlrev_b32_e32 v30, 16, v48
	v_and_b32_e32 v31, 0xffff0000, v48
	v_lshlrev_b32_e32 v32, 16, v49
	v_and_b32_e32 v33, 0xffff0000, v49
	s_or_b32 s57, s56, 0x80
	s_addk_i32 s56, 0xff80
	ds_write_b128 v177, v[30:33] offset:128
	v_lshlrev_b32_e32 v30, 16, v42
	v_and_b32_e32 v31, 0xffff0000, v42
	v_lshlrev_b32_e32 v32, 16, v43
	v_and_b32_e32 v33, 0xffff0000, v43
	s_cmp_lt_u32 s79, 4
	ds_write_b128 v177, v[30:33] offset:64
	v_lshlrev_b32_e32 v30, 16, v44
	v_and_b32_e32 v31, 0xffff0000, v44
	v_lshlrev_b32_e32 v32, 16, v45
	v_and_b32_e32 v33, 0xffff0000, v45
	s_cselect_b32 s56, s57, s56
	ds_write_b128 v177, v[30:33] offset:144
	ds_write_b128 v178, v[22:25] offset:1280
	s_cselect_b32 s58, s81, 0x1000
	v_or_b32_e32 v22, s56, v131
	v_xad_u32 v23, v22, -1, s58
	v_cndmask_b32_e64 v22, v23, v22, s[38:39]
	v_or_b32_e32 v23, s56, v135
	v_xad_u32 v24, v23, -1, s58
	v_cndmask_b32_e64 v24, v24, v23, s[38:39]
	v_or_b32_e32 v23, s56, v141
	v_xad_u32 v25, v23, -1, s58
	s_cselect_b32 s59, s3, s78
	v_cndmask_b32_e64 v30, v25, v23, s[38:39]
	v_or_b32_e32 v23, s56, v161
	v_xad_u32 v25, v23, -1, s58
	v_add_u32_e32 v22, s59, v22
	v_add_u32_e32 v30, s59, v30
	v_cndmask_b32_e64 v32, v25, v23, s[38:39]
	v_ashrrev_i32_e32 v23, 31, v22
	v_add_u32_e32 v24, s59, v24
	v_ashrrev_i32_e32 v31, 31, v30
	v_ashrrev_i32_e32 v25, 31, v24
	v_lshlrev_b64 v[30:31], 10, v[30:31]
	v_lshlrev_b64 v[22:23], 12, v[22:23]
	v_lshl_add_u64 v[42:43], v[30:31], 0, v[150:151]
	v_add_u32_e32 v90, s59, v32
	v_lshl_add_u64 v[22:23], v[152:153], 0, v[22:23]
	v_lshlrev_b64 v[24:25], 12, v[24:25]
	v_readlane_b32 s56, v246, 16
	v_lshl_add_u64 v[24:25], v[152:153], 0, v[24:25]
	global_load_dwordx4 v[30:33], v[22:23], off
	global_load_dwordx4 v[38:41], v[24:25], off
	v_lshlrev_b64 v[22:23], 1, v[42:43]
	v_readlane_b32 s66, v246, 26
	v_readlane_b32 s67, v246, 27
	v_readlane_b32 s62, v246, 22
	v_readlane_b32 s63, v246, 23
	v_lshl_add_u64 v[24:25], s[66:67], 0, v[22:23]
	global_load_dwordx4 v[54:57], v[24:25], off
	v_lshl_add_u64 v[24:25], s[84:85], 0, v[22:23]
	v_ashrrev_i32_e32 v91, 31, v90
	global_load_dwordx4 v[50:53], v[24:25], off
	v_lshl_add_u64 v[24:25], s[92:93], 0, v[22:23]
	v_lshl_add_u64 v[22:23], s[62:63], 0, v[22:23]
	global_load_dwordx4 v[42:45], v[22:23], off
	v_lshlrev_b64 v[22:23], 12, v[90:91]
	v_lshl_add_u64 v[22:23], v[154:155], 0, v[22:23]
	global_load_dwordx4 v[46:49], v[24:25], off
	s_add_i32 s97, s80, s33
	global_load_dwordx4 v[22:25], v[22:23], off
	s_min_i32 s72, s97, 0x324ff
	v_readlane_b32 s57, v246, 17
	v_readlane_b32 s58, v246, 18
	v_readlane_b32 s59, v246, 19
	v_readlane_b32 s60, v246, 20
	v_readlane_b32 s61, v246, 21
	v_readlane_b32 s64, v246, 24
	v_readlane_b32 s65, v246, 25
	s_cmpk_gt_i32 s97, 0x19ff
	s_mov_b64 s[62:63], -1
	v_readlane_b32 s68, v246, 28
	v_readlane_b32 s69, v246, 29
	v_readlane_b32 s70, v246, 30
	v_readlane_b32 s71, v246, 31
	s_cbranch_scc0 .LBB0_713
	s_cmpk_gt_u32 s97, 0x21ff
	s_cbranch_scc0 .LBB0_710
	s_cmpk_gt_u32 s97, 0x4dff
	s_cbranch_scc0 .LBB0_707
	s_cmpk_gt_u32 s97, 0x63ff
	s_cbranch_scc0 .LBB0_704
	s_mov_b64 s[58:59], -1
	s_cmpk_gt_u32 s97, 0x7cff
	s_cbranch_scc0 .LBB0_701
	s_cmpk_gt_u32 s97, 0x84ff
	s_cbranch_scc0 .LBB0_698
	s_cmp_gt_u32 s97, 0x244ff
	s_mov_b64 s[56:57], -1
	s_cbranch_scc0 .LBB0_696
	s_add_i32 s56, s72, 0xbb00
	s_bfe_u32 s57, s56, 0x6000a
	s_mulk_i32 s57, 0x2493
	s_lshr_b32 s74, s57, 16
	s_mul_i32 s57, s74, 0x1c00
	s_sub_i32 s56, s56, s57
	s_bfe_u32 s65, s56, 0x50001
	s_bfe_u32 s64, s56, 0xa0006
	s_lshl_b32 s64, s64, 1
	s_and_b32 s56, s56, 1
	s_or_b32 s64, s64, s56
	s_mov_b64 s[56:57], 0

; __device__ __forceinline__ ConvTile conv_tile_desc(const unsigned long long* tab, int t) {
;     ...
;     else { const int u = (t < CT_TOTAL ? t : CT_TOTAL - 1) - CT_C; e = u / 7168; const int v = u % 7168; si = 9; di = 17; N = DM; K = EXD; nb = v & 31; kb = v >> 5; }
;     const int n0 = nb * 64;
;     int col0 = n0, nvalid = 64;
;     if (mode) { col0 = (n0 >> 8) * 128 + (n0 & 127); si += (n0 >> 7) & 1; }
;     if (npad) { nvalid = N - n0; if (nvalid <= 0) col0 = 0; }
;     ConvTile c;
;     const size_t KN = (size_t)K * N;
;     c.src = (const float*)tab[si] + (size_t)e * KN + (size_t)(kb * 32) * N + col0;
;     c.dst = (bf16_t*)tab[di] + (size_t)e * (mode ? 2 * KN : KN) + (size_t)n0 * K + kb * 32;
.LBB0_715:
	s_lshl_b32 s62, s65, 6
	s_sub_i32 s61, s96, s62
	s_and_b64 s[58:59], s[58:59], exec
	s_cselect_b32 s63, 64, s61
	s_lshl_b32 s58, s75, 3
	s_add_i32 s58, s58, 0
	s_add_i32 s58, s58, 0x20040
	v_mov_b32_e32 v90, s58
	s_mul_i32 s72, s56, s96
	ds_read_b64 v[90:91], v90
	s_lshl_b64 s[58:59], s[72:73], s60
	s_lshl_b32 s60, s64, 5
	s_mul_i32 s59, s59, s74
	s_mul_hi_u32 s64, s58, s74
	s_add_i32 s59, s64, s59
	s_mul_i32 s58, s58, s74
	s_lshl_b64 s[58:59], s[58:59], 1
	s_waitcnt lgkmcnt(0)
	v_lshl_add_u64 v[90:91], v[90:91], 0, s[58:59]
	s_ashr_i32 s58, s62, 31
	s_mul_i32 s58, s56, s58
	s_mul_hi_u32 s59, s56, s62
	s_add_i32 s58, s59, s58
	s_mul_i32 s59, s57, s62
	s_add_i32 s59, s58, s59
	s_mul_i32 s58, s56, s62
	s_ashr_i32 s61, s60, 31
	s_lshl_b64 s[58:59], s[58:59], 1
	v_lshl_add_u64 v[90:91], v[90:91], 0, s[58:59]
	s_lshl_b64 s[58:59], s[60:61], 1
	v_mul_u32_u24_e32 v92, s56, v130
	v_lshl_add_u64 v[90:91], v[90:91], 0, s[58:59]
	v_lshlrev_b32_e32 v132, 1, v92
	v_lshl_add_u64 v[90:91], v[90:91], 0, v[132:133]
	v_lshlrev_b32_e32 v132, 1, v140
	v_cvt_pk_bf16_f32 v58, v58, v62
	v_cvt_pk_bf16_f32 v62, v66, v70
	v_cvt_pk_bf16_f32 v66, v74, v78
	v_cvt_pk_bf16_f32 v70, v82, v86
	v_cmp_gt_i32_e32 vcc, s63, v130
	v_lshl_add_u64 v[94:95], v[90:91], 0, v[132:133]
	s_lshl_b64 s[56:57], s[56:57], 1
	v_cndmask_b32_e32 v93, 0, v70, vcc
	v_cndmask_b32_e32 v92, 0, v66, vcc
	v_cndmask_b32_e32 v91, 0, v62, vcc
	v_cndmask_b32_e32 v90, 0, v58, vcc
	v_cvt_pk_bf16_f32 v58, v59, v63
	v_cvt_pk_bf16_f32 v59, v67, v71
	v_cvt_pk_bf16_f32 v62, v75, v79
	v_cvt_pk_bf16_f32 v63, v83, v87
	global_store_dwordx4 v[94:95], v[90:93], off nt
	v_cvt_pk_bf16_f32 v60, v60, v64
	v_cvt_pk_bf16_f32 v64, v84, v88
	v_cndmask_b32_e32 v93, 0, v63, vcc
	v_cndmask_b32_e32 v92, 0, v62, vcc
	v_cndmask_b32_e32 v91, 0, v59, vcc
	v_cndmask_b32_e32 v90, 0, v58, vcc
	v_lshl_add_u64 v[58:59], v[94:95], 0, s[56:57]
	v_cvt_pk_bf16_f32 v62, v68, v72
	v_cvt_pk_bf16_f32 v63, v76, v80
	s_add_i32 s33, s88, s33
	global_store_dwordx4 v[58:59], v[90:93], off nt
	s_min_i32 s72, s33, 0x324ff
	s_cmpk_gt_i32 s33, 0x19ff
	v_cndmask_b32_e32 v93, 0, v64, vcc
	v_cndmask_b32_e32 v92, 0, v63, vcc
	v_cndmask_b32_e32 v91, 0, v62, vcc
	v_cndmask_b32_e32 v90, 0, v60, vcc
	v_lshl_add_u64 v[62:63], v[58:59], 0, s[56:57]
	v_cvt_pk_bf16_f32 v58, v61, v65
	v_cvt_pk_bf16_f32 v59, v69, v73
	v_cvt_pk_bf16_f32 v60, v77, v81
	v_cvt_pk_bf16_f32 v61, v85, v89
	global_store_dwordx4 v[62:63], v[90:93], off nt
	v_cndmask_b32_e32 v61, 0, v61, vcc
	v_cndmask_b32_e32 v60, 0, v60, vcc
	v_cndmask_b32_e32 v59, 0, v59, vcc
	v_cndmask_b32_e32 v58, 0, v58, vcc
	v_lshl_add_u64 v[62:63], v[62:63], 0, s[56:57]
	s_mov_b64 s[96:97], -1
	global_store_dwordx4 v[62:63], v[58:61], off nt
	s_cbranch_scc0 .LBB0_740
	s_cmpk_gt_u32 s33, 0x21ff
	s_cbranch_scc0 .LBB0_737
	s_cmpk_gt_u32 s33, 0x4dff
	s_cbranch_scc0 .LBB0_734
	s_cmpk_gt_u32 s33, 0x63ff
	s_cbranch_scc0 .LBB0_731
	s_mov_b64 s[58:59], -1
	s_cmpk_gt_u32 s33, 0x7cff
	s_cbranch_scc0 .LBB0_728
	s_cmpk_gt_u32 s33, 0x84ff
	s_cbranch_scc0 .LBB0_725
	s_mov_b64 s[60:61], -1
	s_cmp_gt_u32 s33, 0x244ff
	s_mov_b64 s[56:57], -1
	s_cbranch_scc0 .LBB0_723
	s_add_i32 s56, s72, 0xbb00
	s_bfe_u32 s57, s56, 0x6000a
	s_mulk_i32 s57, 0x2493
	s_lshr_b32 s64, s57, 16
	s_mul_i32 s57, s64, 0x1c00
	s_sub_i32 s56, s56, s57
	s_bfe_u32 s75, s56, 0x50001
	s_bfe_u32 s74, s56, 0xa0006
	s_lshl_b32 s74, s74, 1
	s_and_b32 s56, s56, 1
	s_or_b32 s74, s74, s56
	s_mov_b64 s[56:57], 0

; __device__ __forceinline__ ConvTile conv_tile_desc(const unsigned long long* tab, int t) {
;     ...
;     else { const int u = (t < CT_TOTAL ? t : CT_TOTAL - 1) - CT_C; e = u / 7168; const int v = u % 7168; si = 9; di = 17; N = DM; K = EXD; nb = v & 31; kb = v >> 5; }
;     const int n0 = nb * 64;
;     int col0 = n0, nvalid = 64;
;     if (mode) { col0 = (n0 >> 8) * 128 + (n0 & 127); si += (n0 >> 7) & 1; }
;     if (npad) { nvalid = N - n0; if (nvalid <= 0) col0 = 0; }
;     ConvTile c;
;     const size_t KN = (size_t)K * N;
;     c.src = (const float*)tab[si] + (size_t)e * KN + (size_t)(kb * 32) * N + col0;
;     c.dst = (bf16_t*)tab[di] + (size_t)e * (mode ? 2 * KN : KN) + (size_t)n0 * K + kb * 32;
;     c.N = N; c.K = K; c.nvalid = nvalid;
;     return c;
; }
.Lcv1_start:
	v_and_b32_e32 v96, 63, v0
	v_lshrrev_b32_e32 v97, 6, v0
	v_lshrrev_b32_e32 v98, 4, v96
	v_and_b32_e32 v99, 15, v96
	v_readfirstlane_b32 s2, v97
	v_lshlrev_b32_e32 v100, 16, v98
	v_lshl_add_u32 v100, v99, 4, v100
	v_add_u32_e32 v101, 0x2000, v100
	v_add_u32_e32 v102, 0x4000, v100
	v_add_u32_e32 v103, 0x6000, v100
	v_add_u32_e32 v104, 0x8000, v100
	v_add_u32_e32 v105, 0xa000, v100
	v_add_u32_e32 v106, 0xc000, v100
	v_add_u32_e32 v107, 0xe000, v100
	v_mul_u32_u24_e32 v108, 0xe000, v99
	v_lshl_add_u32 v108, v98, 4, v108
	v_add_u32_e32 v109, 0x3800, v108
	v_add_u32_e32 v110, 0x7000, v108
	v_add_u32_e32 v111, 0xa800, v108
	v_mov_b32_e32 v112, 0x20088
	v_mov_b32_e32 v113, 0x200c8
	ds_read_b64 v[114:115], v112
	ds_read_b64 v[116:117], v113
	s_waitcnt lgkmcnt(0)
	v_readfirstlane_b32 s4, v114
	v_readfirstlane_b32 s5, v115
	v_readfirstlane_b32 s6, v116
	v_readfirstlane_b32 s7, v117
	s_sub_i32 s3, s90, 216
	s_lshl_b32 s3, s3, 3
	s_add_i32 s3, s3, s2
	s_add_i32 s3, s3, 0x2e400
	s_nop 4
	s_min_u32 s12, s3, 0x324ff
	s_sub_u32 s12, s12, 0x24500
	s_lshr_b32 s13, s12, 10
	s_mul_i32 s13, s13, 37
	s_lshr_b32 s13, s13, 8
	s_mul_i32 s28, s13, 0x1c00
	s_sub_u32 s12, s12, s28
	s_bfe_u32 s28, s12, 0x50001
	s_and_b32 s32, s12, 1
	s_lshr_b32 s12, s12, 6
	s_lshl_b32 s12, s12, 1
	s_or_b32 s12, s12, s32
	s_mul_i32 s29, s13, 0x3800000
	s_lshl_b32 s32, s12, 18
	s_add_u32 s29, s29, s32
	s_lshl_b32 s32, s28, 8
	s_add_u32 s29, s29, s32
	s_add_u32 s8, s4, s29
	s_addc_u32 s9, s5, 0
	s_mul_i32 s29, s13, 0x1c00000
	s_mul_i32 s32, s28, 0xe0000
	s_add_u32 s29, s29, s32
	s_lshl_b32 s32, s12, 6
	s_add_u32 s29, s29, s32
	s_add_u32 s10, s6, s29
	s_addc_u32 s11, s7, 0
	s_nop 0
	global_load_dwordx4 v[128:131], v100, s[8:9] nt
	global_load_dwordx4 v[132:135], v101, s[8:9] nt
	global_load_dwordx4 v[136:139], v102, s[8:9] nt
	global_load_dwordx4 v[140:143], v103, s[8:9] nt
	global_load_dwordx4 v[144:147], v104, s[8:9] nt
	global_load_dwordx4 v[148:151], v105, s[8:9] nt
	global_load_dwordx4 v[152:155], v106, s[8:9] nt
	global_load_dwordx4 v[156:159], v107, s[8:9] nt
	s_add_i32 s3, s3, 320
	s_min_u32 s12, s3, 0x324ff
	s_sub_u32 s12, s12, 0x24500
	s_lshr_b32 s13, s12, 10
	s_mul_i32 s13, s13, 37
	s_lshr_b32 s13, s13, 8
	s_mul_i32 s28, s13, 0x1c00
	s_sub_u32 s12, s12, s28
	s_bfe_u32 s28, s12, 0x50001
	s_and_b32 s32, s12, 1
	s_lshr_b32 s12, s12, 6
	s_lshl_b32 s12, s12, 1
	s_or_b32 s12, s12, s32
	s_mul_i32 s29, s13, 0x3800000
	s_lshl_b32 s32, s12, 18
	s_add_u32 s29, s29, s32
	s_lshl_b32 s32, s28, 8
	s_add_u32 s29, s29, s32
	s_add_u32 s8, s4, s29
	s_addc_u32 s9, s5, 0
	s_mul_i32 s29, s13, 0x1c00000
	s_mul_i32 s32, s28, 0xe0000
	s_add_u32 s29, s29, s32
	s_lshl_b32 s32, s12, 6
	s_add_u32 s29, s29, s32
	s_add_u32 s36, s6, s29
	s_addc_u32 s37, s7, 0
	s_nop 0
	global_load_dwordx4 v[64:67], v100, s[8:9] nt
	global_load_dwordx4 v[68:71], v101, s[8:9] nt
	global_load_dwordx4 v[72:75], v102, s[8:9] nt
	global_load_dwordx4 v[76:79], v103, s[8:9] nt
	global_load_dwordx4 v[80:83], v104, s[8:9] nt
	global_load_dwordx4 v[84:87], v105, s[8:9] nt
	global_load_dwordx4 v[88:91], v106, s[8:9] nt
	global_load_dwordx4 v[92:95], v107, s[8:9] nt
	s_waitcnt vmcnt(8)
	v_cvt_pk_bf16_f32 v112, v128, v132
	v_cvt_pk_bf16_f32 v113, v136, v140
	v_cvt_pk_bf16_f32 v114, v144, v148
	v_cvt_pk_bf16_f32 v115, v152, v156
	global_store_dwordx4 v108, v[112:115], s[10:11] nt
	v_cvt_pk_bf16_f32 v116, v129, v133
	v_cvt_pk_bf16_f32 v117, v137, v141
	v_cvt_pk_bf16_f32 v118, v145, v149
	v_cvt_pk_bf16_f32 v119, v153, v157
	global_store_dwordx4 v109, v[116:119], s[10:11] nt
	v_cvt_pk_bf16_f32 v120, v130, v134
	v_cvt_pk_bf16_f32 v121, v138, v142
	v_cvt_pk_bf16_f32 v122, v146, v150
	v_cvt_pk_bf16_f32 v123, v154, v158
	global_store_dwordx4 v110, v[120:123], s[10:11] nt
	v_cvt_pk_bf16_f32 v96, v131, v135
	v_cvt_pk_bf16_f32 v97, v139, v143
	v_cvt_pk_bf16_f32 v98, v147, v151
	v_cvt_pk_bf16_f32 v99, v155, v159
	global_store_dwordx4 v111, v[96:99], s[10:11] nt
	s_movk_i32 s33, 25
; __device__ __forceinline__ ConvTile conv_tile_desc(const unsigned long long* tab, int t) {
;     ...
;     else { const int u = (t < CT_TOTAL ? t : CT_TOTAL - 1) - CT_C; e = u / 7168; const int v = u % 7168; si = 9; di = 17; N = DM; K = EXD; nb = v & 31; kb = v >> 5; }
;     const int n0 = nb * 64;
;     int col0 = n0, nvalid = 64;
;     if (mode) { col0 = (n0 >> 8) * 128 + (n0 & 127); si += (n0 >> 7) & 1; }
;     if (npad) { nvalid = N - n0; if (nvalid <= 0) col0 = 0; }
;     ConvTile c;
;     const size_t KN = (size_t)K * N;
;     c.src = (const float*)tab[si] + (size_t)e * KN + (size_t)(kb * 32) * N + col0;
;     c.dst = (bf16_t*)tab[di] + (size_t)e * (mode ? 2 * KN : KN) + (size_t)n0 * K + kb * 32;
;     c.N = N; c.K = K; c.nvalid = nvalid;
;     return c;
; }
.Lcv1_loop:
	s_add_i32 s3, s3, 320
	s_min_u32 s12, s3, 0x324ff
	s_sub_u32 s12, s12, 0x24500
	s_lshr_b32 s13, s12, 10
	s_mul_i32 s13, s13, 37
	s_lshr_b32 s13, s13, 8
	s_mul_i32 s28, s13, 0x1c00
	s_sub_u32 s12, s12, s28
	s_bfe_u32 s28, s12, 0x50001
	s_and_b32 s32, s12, 1
	s_lshr_b32 s12, s12, 6
	s_lshl_b32 s12, s12, 1
	s_or_b32 s12, s12, s32
	s_mul_i32 s29, s13, 0x3800000
	s_lshl_b32 s32, s12, 18
	s_add_u32 s29, s29, s32
	s_lshl_b32 s32, s28, 8
	s_add_u32 s29, s29, s32
	s_add_u32 s8, s4, s29
	s_addc_u32 s9, s5, 0
	s_mul_i32 s29, s13, 0x1c00000
	s_mul_i32 s32, s28, 0xe0000
	s_add_u32 s29, s29, s32
	s_lshl_b32 s32, s12, 6
	s_add_u32 s29, s29, s32
	s_add_u32 s10, s6, s29
	s_addc_u32 s11, s7, 0
	s_nop 0
	global_load_dwordx4 v[128:131], v100, s[8:9] nt
	global_load_dwordx4 v[132:135], v101, s[8:9] nt
	global_load_dwordx4 v[136:139], v102, s[8:9] nt
	global_load_dwordx4 v[140:143], v103, s[8:9] nt
	global_load_dwordx4 v[144:147], v104, s[8:9] nt
	global_load_dwordx4 v[148:151], v105, s[8:9] nt
	global_load_dwordx4 v[152:155], v106, s[8:9] nt
	global_load_dwordx4 v[156:159], v107, s[8:9] nt
	s_waitcnt vmcnt(12)
	v_cvt_pk_bf16_f32 v112, v64, v68
	v_cvt_pk_bf16_f32 v113, v72, v76
	v_cvt_pk_bf16_f32 v114, v80, v84
	v_cvt_pk_bf16_f32 v115, v88, v92
	global_store_dwordx4 v108, v[112:115], s[36:37] nt
	v_cvt_pk_bf16_f32 v116, v65, v69
	v_cvt_pk_bf16_f32 v117, v73, v77
	v_cvt_pk_bf16_f32 v118, v81, v85
	v_cvt_pk_bf16_f32 v119, v89, v93
	global_store_dwordx4 v109, v[116:119], s[36:37] nt
	v_cvt_pk_bf16_f32 v120, v66, v70
	v_cvt_pk_bf16_f32 v121, v74, v78
	v_cvt_pk_bf16_f32 v122, v82, v86
	v_cvt_pk_bf16_f32 v123, v90, v94
	global_store_dwordx4 v110, v[120:123], s[36:37] nt
	v_cvt_pk_bf16_f32 v96, v67, v71
	v_cvt_pk_bf16_f32 v97, v75, v79
	v_cvt_pk_bf16_f32 v98, v83, v87
	v_cvt_pk_bf16_f32 v99, v91, v95
	global_store_dwordx4 v111, v[96:99], s[36:37] nt
	s_add_i32 s3, s3, 320
	s_min_u32 s12, s3, 0x324ff
	s_sub_u32 s12, s12, 0x24500
	s_lshr_b32 s13, s12, 10
	s_mul_i32 s13, s13, 37
	s_lshr_b32 s13, s13, 8
	s_mul_i32 s28, s13, 0x1c00
	s_sub_u32 s12, s12, s28
	s_bfe_u32 s28, s12, 0x50001
	s_and_b32 s32, s12, 1
	s_lshr_b32 s12, s12, 6
	s_lshl_b32 s12, s12, 1
	s_or_b32 s12, s12, s32
	s_mul_i32 s29, s13, 0x3800000
	s_lshl_b32 s32, s12, 18
	s_add_u32 s29, s29, s32
	s_lshl_b32 s32, s28, 8
	s_add_u32 s29, s29, s32
	s_add_u32 s8, s4, s29
	s_addc_u32 s9, s5, 0
	s_mul_i32 s29, s13, 0x1c00000
	s_mul_i32 s32, s28, 0xe0000
	s_add_u32 s29, s29, s32
	s_lshl_b32 s32, s12, 6
	s_add_u32 s29, s29, s32
	s_add_u32 s36, s6, s29
	s_addc_u32 s37, s7, 0
	s_nop 0
	global_load_dwordx4 v[64:67], v100, s[8:9] nt
	global_load_dwordx4 v[68:71], v101, s[8:9] nt
	global_load_dwordx4 v[72:75], v102, s[8:9] nt
	global_load_dwordx4 v[76:79], v103, s[8:9] nt
	global_load_dwordx4 v[80:83], v104, s[8:9] nt
	global_load_dwordx4 v[84:87], v105, s[8:9] nt
	global_load_dwordx4 v[88:91], v106, s[8:9] nt
	global_load_dwordx4 v[92:95], v107, s[8:9] nt
	s_waitcnt vmcnt(12)
	v_cvt_pk_bf16_f32 v112, v128, v132
	v_cvt_pk_bf16_f32 v113, v136, v140
	v_cvt_pk_bf16_f32 v114, v144, v148
	v_cvt_pk_bf16_f32 v115, v152, v156
	global_store_dwordx4 v108, v[112:115], s[10:11] nt
	v_cvt_pk_bf16_f32 v116, v129, v133
	v_cvt_pk_bf16_f32 v117, v137, v141
	v_cvt_pk_bf16_f32 v118, v145, v149
	v_cvt_pk_bf16_f32 v119, v153, v157
	global_store_dwordx4 v109, v[116:119], s[10:11] nt
	v_cvt_pk_bf16_f32 v120, v130, v134
	v_cvt_pk_bf16_f32 v121, v138, v142
	v_cvt_pk_bf16_f32 v122, v146, v150
	v_cvt_pk_bf16_f32 v123, v154, v158
	global_store_dwordx4 v110, v[120:123], s[10:11] nt
	v_cvt_pk_bf16_f32 v96, v131, v135
	v_cvt_pk_bf16_f32 v97, v139, v143
	v_cvt_pk_bf16_f32 v98, v147, v151
	v_cvt_pk_bf16_f32 v99, v155, v159
	global_store_dwordx4 v111, v[96:99], s[10:11] nt
	s_sub_i32 s33, s33, 1
	s_cmp_lg_u32 s33, 0
	s_cbranch_scc1 .Lcv1_loop
	s_waitcnt vmcnt(4)
	v_cvt_pk_bf16_f32 v112, v64, v68
	v_cvt_pk_bf16_f32 v113, v72, v76
	v_cvt_pk_bf16_f32 v114, v80, v84
	v_cvt_pk_bf16_f32 v115, v88, v92
	global_store_dwordx4 v108, v[112:115], s[36:37] nt
	v_cvt_pk_bf16_f32 v116, v65, v69
	v_cvt_pk_bf16_f32 v117, v73, v77
	v_cvt_pk_bf16_f32 v118, v81, v85
	v_cvt_pk_bf16_f32 v119, v89, v93
	global_store_dwordx4 v109, v[116:119], s[36:37] nt
	v_cvt_pk_bf16_f32 v120, v66, v70
	v_cvt_pk_bf16_f32 v121, v74, v78
	v_cvt_pk_bf16_f32 v122, v82, v86
	v_cvt_pk_bf16_f32 v123, v90, v94
	global_store_dwordx4 v110, v[120:123], s[36:37] nt
	v_cvt_pk_bf16_f32 v96, v67, v71
	v_cvt_pk_bf16_f32 v97, v75, v79
	v_cvt_pk_bf16_f32 v98, v83, v87
	v_cvt_pk_bf16_f32 v99, v91, v95
	global_store_dwordx4 v111, v[96:99], s[36:37] nt
	s_branch .LBB0_1389
